# baseline (speedup 1.0000x reference)
_ZN12_GLOBAL__N_113search_kernelEPKfS1_PhPf:
	s_load_dwordx2 s[8:9], s[0:1], 0x0
	s_load_dwordx2 s[4:5], s[0:1], 0x10
	s_load_dwordx2 s[20:21], s[0:1], 0x8
	s_movk_i32 s3, 0x90
	v_readfirstlane_b32 s10, v0
	v_cmp_gt_u32_e32 vcc, s3, v0
	s_and_saveexec_b64 s[6:7], vcc
	v_mov_b32_e32 v2, -1
	v_lshlrev_b32_e32 v1, 3, v0
	v_mov_b32_e32 v3, v2
	ds_write_b64 v1, v[2:3] offset:16384
	s_or_b64 exec, exec, s[6:7]
	s_waitcnt lgkmcnt(0)
	s_sub_u32 s22, s20, s8
	s_subb_u32 s23, s21, s9
	s_add_u32 s6, s4, 0x240000
	s_addc_u32 s7, s5, 0
	s_lshl_b32 s11, s2, 1
	s_and_b32 s14, s11, 14
	s_ashr_i32 s11, s2, 7
	s_lshr_b32 s15, s10, 6
	s_add_i32 s14, s14, s11
	s_bfe_u32 s2, s2, 0x40003
	s_mul_i32 s11, s15, 24
	v_mul_u32_u24_e32 v2, 0x71d, v0
	v_mul_u32_u24_e32 v4, 0x195, v0
	s_min_u32 s18, s11, 0xa5
	s_mul_i32 s11, s14, 3
	s_mul_i32 s12, s2, 9
	s_mov_b32 s13, 0
	v_lshrrev_b32_e32 v3, 16, v2
	s_movk_i32 s19, 0xffdc
	v_lshrrev_b32_e32 v5, 17, v4
	v_mad_i32_i24 v2, v3, s19, v0
	v_mad_i32_i24 v4, v5, -9, v3
	v_add_u32_e32 v3, s11, v5
	v_mov_b64_e32 v[6:7], s[12:13]
	v_mad_i64_i32 v[8:9], s[16:17], v3, s3, v[6:7]
	v_ashrrev_i32_e32 v5, 31, v4
	v_lshl_add_u64 v[4:5], v[8:9], 0, v[4:5]
	s_movk_i32 s13, 0x240
	v_mov_b64_e32 v[8:9], s[8:9]
	v_mad_u64_u32 v[10:11], s[8:9], v4, s13, v[8:9]
	v_min_u32_e32 v4, 0x1cb, v0
	v_or_b32_e32 v4, 0x200, v4
	v_mad_i32_i24 v11, v5, s13, v11
	v_mul_u32_u24_e32 v5, 0x71d, v4
	v_ashrrev_i32_e32 v3, 31, v2
	v_lshrrev_b32_e32 v5, 16, v5
	v_lshl_add_u64 v[2:3], v[2:3], 4, v[10:11]
	v_mad_i32_i24 v10, v5, s19, v4
	v_mul_u32_u24_e32 v4, 0x653, v4
	v_lshrrev_b32_e32 v11, 19, v4
	v_mad_i32_i24 v4, v11, -9, v5
	v_add_u32_e32 v5, s11, v11
	v_mad_i64_i32 v[6:7], s[8:9], v5, s3, v[6:7]
	v_ashrrev_i32_e32 v5, 31, v4
	v_lshl_add_u64 v[4:5], v[6:7], 0, v[4:5]
	v_mad_u64_u32 v[12:13], s[8:9], v4, s13, v[8:9]
	s_mul_i32 s8, s14, 0x90
	s_barrier
	v_lshl_add_u64 v[244:245], v[2:3], 0, s[22:23]
	global_load_dwordx4 v[6:9], v[2:3], off
	s_add_i32 s3, s8, s12
	v_and_b32_e32 v210, 15, v0
	v_lshlrev_b32_e32 v252, 3, v210
	v_bfe_u32 v253, v0, 4, 2
	s_lshl_b32 s11, s3, 6
	v_and_b32_e32 v2, 48, v0
	s_mul_i32 s9, s14, 0xbd
	v_or3_b32 v2, s11, v2, v210
	s_add_i32 s18, s18, s9
	v_and_b32_e32 v1, 63, v0
	v_ashrrev_i32_e32 v3, 31, v2
	s_lshl_b32 s3, s18, 6
	v_mad_i32_i24 v13, v5, s13, v13
	v_lshl_add_u64 v[14:15], v[2:3], 4, s[4:5]
	v_or_b32_e32 v2, s3, v1
	v_ashrrev_i32_e32 v11, 31, v10
	v_ashrrev_i32_e32 v3, 31, v2
	v_lshl_add_u64 v[10:11], v[10:11], 4, v[12:13]
	v_lshl_add_u64 v[16:17], v[2:3], 4, s[6:7]
	global_load_dwordx4 v[2:5], v[14:15], off
	global_load_dwordx4 v[58:61], v[16:17], off nt
	s_add_i32 s12, s3, 64
	v_lshl_add_u64 v[246:247], v[10:11], 0, s[22:23]
	global_load_dwordx4 v[10:13], v[10:11], off
	v_or_b32_e32 v14, s12, v1
	v_ashrrev_i32_e32 v15, 31, v14
	v_lshl_add_u64 v[14:15], v[14:15], 4, s[6:7]
	s_add_i32 s12, s3, 0x80
	global_load_dwordx4 v[54:57], v[14:15], off nt
	v_or_b32_e32 v14, s12, v1
	v_ashrrev_i32_e32 v15, 31, v14
	v_lshl_add_u64 v[14:15], v[14:15], 4, s[6:7]
	s_add_i32 s12, s3, 0xc0
	global_load_dwordx4 v[98:101], v[14:15], off nt
	v_or_b32_e32 v14, s12, v1
	v_ashrrev_i32_e32 v15, 31, v14
	v_lshl_add_u64 v[14:15], v[14:15], 4, s[6:7]
	s_add_i32 s12, s11, 64
	global_load_dwordx4 v[82:85], v[14:15], off nt
	v_or_b32_e32 v14, s12, v1
	v_ashrrev_i32_e32 v15, 31, v14
	v_lshl_add_u64 v[14:15], v[14:15], 4, s[4:5]
	s_add_i32 s12, s11, 0x80
	global_load_dwordx4 v[34:37], v[14:15], off
	v_or_b32_e32 v14, s12, v1
	s_add_i32 s12, s11, 0xc0
	v_or_b32_e32 v16, s12, v1
	s_add_i32 s12, s11, 0x100
	v_or_b32_e32 v18, s12, v1
	s_add_i32 s12, s11, 0x140
	v_ashrrev_i32_e32 v15, 31, v14
	v_ashrrev_i32_e32 v17, 31, v16
	v_or_b32_e32 v20, s12, v1
	v_lshl_add_u64 v[14:15], v[14:15], 4, s[4:5]
	v_lshl_add_u64 v[16:17], v[16:17], 4, s[4:5]
	v_ashrrev_i32_e32 v21, 31, v20
	s_add_i32 s12, s11, 0x180
	global_load_dwordx4 v[30:33], v[14:15], off
	global_load_dwordx4 v[26:29], v[16:17], off
	v_lshl_add_u64 v[14:15], v[20:21], 4, s[4:5]
	v_or_b32_e32 v20, s12, v1
	v_ashrrev_i32_e32 v21, 31, v20
	s_add_i32 s12, s11, 0x1c0
	v_lshl_add_u64 v[38:39], v[20:21], 4, s[4:5]
	v_or_b32_e32 v20, s12, v1
	v_ashrrev_i32_e32 v21, 31, v20
	s_addk_i32 s11, 0x200
	v_lshl_add_u64 v[40:41], v[20:21], 4, s[4:5]
	v_or_b32_e32 v20, s11, v1
	v_ashrrev_i32_e32 v21, 31, v20
	s_add_i32 s11, s3, 0x100
	v_lshl_add_u64 v[42:43], v[20:21], 4, s[4:5]
	v_or_b32_e32 v20, s11, v1
	s_add_i32 s11, s3, 0x140
	v_or_b32_e32 v16, s11, v1
	v_ashrrev_i32_e32 v17, 31, v16
	s_add_i32 s11, s3, 0x180
	v_lshl_add_u64 v[46:47], v[16:17], 4, s[6:7]
	v_or_b32_e32 v16, s11, v1
	v_ashrrev_i32_e32 v17, 31, v16
	s_add_i32 s11, s3, 0x1c0
	v_lshl_add_u64 v[48:49], v[16:17], 4, s[6:7]
	v_or_b32_e32 v16, s11, v1
	v_ashrrev_i32_e32 v17, 31, v16
	s_add_i32 s11, s3, 0x200
	v_lshl_add_u64 v[50:51], v[16:17], 4, s[6:7]
	v_or_b32_e32 v16, s11, v1
	v_ashrrev_i32_e32 v17, 31, v16
	s_add_i32 s11, s3, 0x240
	v_lshl_add_u64 v[52:53], v[16:17], 4, s[6:7]
	v_or_b32_e32 v16, s11, v1
	v_ashrrev_i32_e32 v17, 31, v16
	s_add_i32 s11, s3, 0x280
	v_ashrrev_i32_e32 v19, 31, v18
	v_ashrrev_i32_e32 v21, 31, v20
	v_lshl_add_u64 v[66:67], v[16:17], 4, s[6:7]
	v_or_b32_e32 v16, s11, v1
	v_lshl_add_u64 v[18:19], v[18:19], 4, s[4:5]
	v_lshl_add_u64 v[44:45], v[20:21], 4, s[6:7]
	v_ashrrev_i32_e32 v17, 31, v16
	s_add_i32 s11, s3, 0x2c0
	global_load_dwordx4 v[22:25], v[18:19], off
	v_lshl_add_u64 v[86:87], v[16:17], 4, s[6:7]
	v_or_b32_e32 v16, s11, v1
	s_add_i32 s11, s3, 0x300
	global_load_dwordx4 v[18:21], v[14:15], off
	global_load_dwordx4 v[62:65], v[44:45], off nt
	v_lshlrev_b32_e32 v14, 4, v0
	s_waitcnt vmcnt(12)
	ds_write_b128 v14, v[6:9]
	v_or_b32_e32 v6, s11, v1
	v_ashrrev_i32_e32 v7, 31, v6
	s_add_i32 s11, s3, 0x340
	v_lshl_add_u64 v[142:143], v[6:7], 4, s[6:7]
	v_or_b32_e32 v6, s11, v1
	v_ashrrev_i32_e32 v7, 31, v6
	s_add_i32 s11, s3, 0x380
	v_lshl_add_u64 v[146:147], v[6:7], 4, s[6:7]
	v_or_b32_e32 v6, s11, v1
	v_ashrrev_i32_e32 v17, 31, v16
	v_ashrrev_i32_e32 v7, 31, v6
	v_lshl_add_u64 v[88:89], v[16:17], 4, s[6:7]
	s_waitcnt vmcnt(9)
	ds_write_b128 v14, v[10:13] offset:8192
	global_load_dwordx4 v[14:17], v[38:39], off
	global_load_dwordx4 v[10:13], v[40:41], off
	v_lshl_add_u64 v[38:39], v[6:7], 4, s[6:7]
	global_load_dwordx4 v[6:9], v[42:43], off
	global_load_dwordx4 v[94:97], v[46:47], off nt
	global_load_dwordx4 v[78:81], v[48:49], off nt
	global_load_dwordx4 v[74:77], v[50:51], off nt
	global_load_dwordx4 v[70:73], v[52:53], off nt
	s_add_i32 s11, s3, 0x3c0
	v_or_b32_e32 v40, s11, v1
	v_ashrrev_i32_e32 v41, 31, v40
	s_lshl_b32 s24, s15, 10
	s_add_i32 s24, s24, 0x46e0
	s_mov_b32 m0, s24
	s_mul_i32 s25, s14, 0xf300
	s_mul_i32 s28, s2, 0xf30
	s_add_i32 s25, s25, s28
	s_add_i32 s25, s25, 0x534000
	s_add_u32 s26, s4, s25
	s_addc_u32 s27, s5, 0
	v_lshlrev_b32_e32 v248, 4, v0
	v_mov_b32_e32 v249, 0
	v_lshl_add_u64 v[248:249], v[248:249], 0, s[26:27]
	s_mul_i32 s25, s14, 0x3cc0
	s_mul_i32 s28, s2, 0x3cc
	s_add_i32 s25, s25, s28
	s_add_i32 s25, s25, 0x627000
	s_add_u32 s26, s4, s25
	s_addc_u32 s27, s5, 0
	v_lshlrev_b32_e32 v242, 2, v0
	v_mov_b32_e32 v243, 0
	v_lshl_add_u64 v[242:243], v[242:243], 0, s[26:27]
	global_load_lds_dwordx4 v[244:245], off
	global_load_lds_dwordx4 v[246:247], off
	global_load_lds_dwordx4 v[248:249], off
	global_load_lds_dword v[242:243], off
	v_mfma_f32_16x16x32_f16 v[102:105], v[58:61], v[2:5], 0
	v_lshl_add_u64 v[40:41], v[40:41], 4, s[6:7]
	global_load_dwordx4 v[66:69], v[66:67], off nt
	s_nop 0
	global_load_dwordx4 v[90:93], v[86:87], off nt
	s_nop 0
	global_load_dwordx4 v[86:89], v[88:89], off nt
	s_nop 0
	global_load_dwordx4 v[50:53], v[142:143], off nt
	global_load_dwordx4 v[46:49], v[146:147], off nt
	global_load_dwordx4 v[42:45], v[38:39], off nt
	s_nop 0
	global_load_dwordx4 v[38:41], v[40:41], off nt
	s_waitcnt vmcnt(22)
	v_mfma_f32_16x16x32_f16 v[106:109], v[54:57], v[2:5], 0
	s_mov_b32 s11, 0x7f000000
	v_mov_b32_e32 v159, 0
	v_mov_b32_e32 v171, 0
	s_waitcnt vmcnt(21)
	v_mfma_f32_16x16x32_f16 v[110:113], v[98:101], v[2:5], 0
	v_mov_b32_e32 v173, 0
	v_mov_b32_e32 v197, 0
	v_mov_b32_e32 v195, 0
	s_waitcnt vmcnt(20)
	v_mfma_f32_16x16x32_f16 v[114:117], v[82:85], v[2:5], 0
	v_mov_b32_e32 v199, 0
	v_min_i32_e32 v102, v102, v103
	v_min_i32_e32 v103, v104, v105
	v_min_i32_e32 v104, v106, v107
	v_min_i32_e32 v105, v108, v109
	v_min_i32_e32 v154, v110, v111
	v_min3_i32 v102, v102, v103, v104
	v_min_i32_e32 v155, v112, v113
	v_min_i32_e32 v114, v114, v115
	v_min3_i32 v102, v102, v105, v154
	s_waitcnt vmcnt(19)
	v_mfma_f32_16x16x32_f16 v[118:121], v[58:61], v[34:37], 0
	v_min_i32_e32 v115, v116, v117
	v_min3_i32 v102, v102, v155, v114
	v_min3_i32 v158, v102, v115, s11
	v_mfma_f32_16x16x32_f16 v[122:125], v[54:57], v[34:37], 0
	v_mov_b32_e32 v204, 0
	s_add_i32 s12, s3, 0x400
	v_mov_b32_e32 v205, 0
	v_mfma_f32_16x16x32_f16 v[126:129], v[98:101], v[34:37], 0
	v_mov_b32_e32 v220, 0
	v_mfma_f32_16x16x32_f16 v[130:133], v[82:85], v[34:37], 0
	s_waitcnt vmcnt(18)
	v_mfma_f32_16x16x32_f16 v[134:137], v[58:61], v[30:33], 0
	v_mfma_f32_16x16x32_f16 v[138:141], v[54:57], v[30:33], 0
	v_mfma_f32_16x16x32_f16 v[142:145], v[98:101], v[30:33], 0
	v_mfma_f32_16x16x32_f16 v[146:149], v[82:85], v[30:33], 0
	s_nop 0
	v_min_i32_e32 v102, v118, v119
	v_min_i32_e32 v103, v120, v121
	v_min_i32_e32 v104, v122, v123
	v_min_i32_e32 v105, v124, v125
	v_min_i32_e32 v114, v126, v127
	v_min3_i32 v102, v102, v103, v104
	v_min_i32_e32 v115, v128, v129
	v_min_i32_e32 v116, v130, v131
	v_min3_i32 v102, v102, v105, v114
	v_min_i32_e32 v117, v132, v133
	v_min3_i32 v102, v102, v115, v116
	s_waitcnt vmcnt(17)
	v_mfma_f32_16x16x32_f16 v[150:153], v[58:61], v[26:29], 0
	v_min3_i32 v170, v102, v117, s11
	v_mfma_f32_16x16x32_f16 v[106:109], v[54:57], v[26:29], 0
	v_mfma_f32_16x16x32_f16 v[110:113], v[98:101], v[26:29], 0
	v_mfma_f32_16x16x32_f16 v[154:157], v[82:85], v[26:29], 0
	s_nop 0
	v_min_i32_e32 v114, v134, v135
	v_min_i32_e32 v115, v136, v137
	v_min_i32_e32 v116, v138, v139
	v_min_i32_e32 v117, v140, v141
	v_min_i32_e32 v122, v142, v143
	v_min3_i32 v114, v114, v115, v116
	v_min_i32_e32 v123, v144, v145
	v_min_i32_e32 v124, v146, v147
	v_min3_i32 v114, v114, v117, v122
	v_min_i32_e32 v125, v148, v149
	v_min3_i32 v114, v114, v123, v124
	s_waitcnt vmcnt(16)
	v_mfma_f32_16x16x32_f16 v[160:163], v[58:61], v[22:25], 0
	v_min3_i32 v172, v114, v125, s11
	v_mfma_f32_16x16x32_f16 v[164:167], v[54:57], v[22:25], 0
	v_mfma_f32_16x16x32_f16 v[118:121], v[98:101], v[22:25], 0
	v_mfma_f32_16x16x32_f16 v[128:131], v[82:85], v[22:25], 0
	s_nop 0
	v_min_i32_e32 v110, v110, v111
	s_waitcnt vmcnt(15)
	v_mfma_f32_16x16x32_f16 v[174:177], v[58:61], v[18:21], 0
	v_min_i32_e32 v111, v112, v113
	v_min_i32_e32 v112, v154, v155
	v_min_i32_e32 v113, v156, v157
	s_waitcnt vmcnt(13)
	v_mfma_f32_16x16x32_f16 v[102:105], v[58:61], v[14:17], 0
	s_waitcnt vmcnt(12)
	v_mfma_f32_16x16x32_f16 v[134:137], v[58:61], v[10:13], 0
	s_waitcnt vmcnt(11)
	v_mfma_f32_16x16x32_f16 v[114:117], v[58:61], v[6:9], 0
	v_min_i32_e32 v58, v150, v151
	v_min_i32_e32 v59, v152, v153
	v_min_i32_e32 v60, v106, v107
	v_min_i32_e32 v61, v108, v109
	v_min3_i32 v58, v58, v59, v60
	v_min3_i32 v58, v58, v61, v110
	v_min3_i32 v58, v58, v111, v112
	v_mfma_f32_16x16x32_f16 v[178:181], v[54:57], v[18:21], 0
	v_min3_i32 v196, v58, v113, s11
	v_mfma_f32_16x16x32_f16 v[182:185], v[98:101], v[18:21], 0
	v_mfma_f32_16x16x32_f16 v[186:189], v[82:85], v[18:21], 0
	s_nop 0
	v_min_i32_e32 v110, v160, v161
	v_min_i32_e32 v111, v162, v163
	v_min_i32_e32 v112, v164, v165
	v_mfma_f32_16x16x32_f16 v[142:145], v[54:57], v[14:17], 0
	v_min_i32_e32 v113, v166, v167
	v_min_i32_e32 v118, v118, v119
	v_min_i32_e32 v119, v120, v121
	v_mfma_f32_16x16x32_f16 v[146:149], v[98:101], v[14:17], 0
	v_min_i32_e32 v120, v128, v129
	v_mfma_f32_16x16x32_f16 v[58:61], v[54:57], v[10:13], 0
	v_mfma_f32_16x16x32_f16 v[122:125], v[54:57], v[6:9], 0
	v_mfma_f32_16x16x32_f16 v[54:57], v[98:101], v[10:13], 0
	v_mfma_f32_16x16x32_f16 v[126:129], v[98:101], v[6:9], 0
	v_min3_i32 v99, v110, v111, v112
	v_min3_i32 v99, v99, v113, v118
	v_min_i32_e32 v98, v130, v131
	v_min3_i32 v99, v99, v119, v120
	v_mfma_f32_16x16x32_f16 v[106:109], v[82:85], v[14:17], 0
	v_min3_i32 v194, v99, v98, s11
	v_mfma_f32_16x16x32_f16 v[138:141], v[82:85], v[10:13], 0
	v_min_i32_e32 v98, v182, v183
	v_min_i32_e32 v99, v184, v185
	v_min_i32_e32 v100, v186, v187
	v_mfma_f32_16x16x32_f16 v[130:133], v[82:85], v[6:9], 0
	v_min_i32_e32 v82, v174, v175
	v_min_i32_e32 v83, v176, v177
	v_min_i32_e32 v84, v178, v179
	v_min_i32_e32 v85, v180, v181
	v_min3_i32 v82, v82, v83, v84
	v_min3_i32 v82, v82, v85, v98
	v_min_i32_e32 v101, v188, v189
	v_min3_i32 v82, v82, v99, v100
	v_min3_i32 v198, v82, v101, s11
	v_mfma_f32_16x16x32_f16 v[150:153], v[62:65], v[2:5], 0
	v_min_i32_e32 v82, v102, v103
	v_min_i32_e32 v83, v104, v105
	v_min_i32_e32 v84, v142, v143
	v_min_i32_e32 v85, v144, v145
	v_min_i32_e32 v98, v146, v147
	v_min3_i32 v82, v82, v83, v84
	v_min_i32_e32 v99, v148, v149
	v_min_i32_e32 v100, v106, v107
	v_min3_i32 v82, v82, v85, v98
	v_min_i32_e32 v101, v108, v109
	v_min3_i32 v82, v82, v99, v100
	v_min3_i32 v203, v82, v101, s11
	v_mfma_f32_16x16x32_f16 v[162:165], v[62:65], v[34:37], 0
	v_min_i32_e32 v58, v58, v59
	v_min_i32_e32 v59, v60, v61
	v_min_i32_e32 v54, v54, v55
	v_mfma_f32_16x16x32_f16 v[166:169], v[62:65], v[30:33], 0
	v_min_i32_e32 v55, v56, v57
	v_min_i32_e32 v56, v138, v139
	v_min_i32_e32 v57, v140, v141
	v_mfma_f32_16x16x32_f16 v[154:157], v[62:65], v[26:29], 0
	v_mfma_f32_16x16x32_f16 v[110:113], v[62:65], v[22:25], 0
	v_mfma_f32_16x16x32_f16 v[118:121], v[62:65], v[18:21], 0
	v_mfma_f32_16x16x32_f16 v[102:105], v[62:65], v[14:17], 0
	v_mfma_f32_16x16x32_f16 v[106:109], v[62:65], v[10:13], 0
	v_mfma_f32_16x16x32_f16 v[98:101], v[62:65], v[6:9], 0
	v_min_i32_e32 v62, v134, v135
	v_min_i32_e32 v63, v136, v137
	v_min3_i32 v58, v62, v63, v58
	v_min3_i32 v54, v58, v59, v54
	v_min3_i32 v54, v54, v55, v56
	v_min3_i32 v202, v54, v57, s11
	v_mov_b32_e32 v54, 0
	s_waitcnt vmcnt(10)
	v_mfma_f32_16x16x32_f16 v[174:177], v[94:97], v[2:5], 0
	v_add_u32_e32 v60, v1, v54
	v_add_u32_e32 v54, s12, v60
	s_add_i32 s12, s3, 0x440
	v_add_u32_e32 v56, s12, v60
	s_add_i32 s12, s3, 0x480
	v_add_u32_e32 v58, s12, v60
	s_add_i32 s12, s3, 0x4c0
	v_ashrrev_i32_e32 v55, 31, v54
	v_ashrrev_i32_e32 v57, 31, v56
	v_ashrrev_i32_e32 v59, 31, v58
	v_add_u32_e32 v60, s12, v60
	s_waitcnt vmcnt(9)
	v_mfma_f32_16x16x32_f16 v[134:137], v[78:81], v[2:5], 0
	v_lshl_add_u64 v[54:55], v[54:55], 4, s[6:7]
	v_lshl_add_u64 v[56:57], v[56:57], 4, s[6:7]
	v_lshl_add_u64 v[58:59], v[58:59], 4, s[6:7]
	s_waitcnt vmcnt(8)
	v_mfma_f32_16x16x32_f16 v[178:181], v[74:77], v[2:5], 0
	v_ashrrev_i32_e32 v61, 31, v60
	v_lshl_add_u64 v[138:139], v[60:61], 4, s[6:7]
	global_load_dwordx4 v[82:85], v[54:55], off nt
	global_load_dwordx4 v[62:65], v[56:57], off nt
	s_nop 0
	global_load_dwordx4 v[58:61], v[58:59], off nt
	s_nop 0
	global_load_dwordx4 v[54:57], v[138:139], off nt
	v_mfma_f32_16x16x32_f16 v[182:185], v[94:97], v[34:37], 0
	v_min_i32_e32 v114, v114, v115
	v_min_i32_e32 v115, v116, v117
	v_min_i32_e32 v116, v122, v123
	v_min_i32_e32 v117, v124, v125
	v_min_i32_e32 v122, v126, v127
	v_min3_i32 v114, v114, v115, v116
	v_min_i32_e32 v123, v128, v129
	v_min_i32_e32 v124, v130, v131
	v_min3_i32 v114, v114, v117, v122
	v_min_i32_e32 v125, v132, v133
	v_min3_i32 v114, v114, v123, v124
	v_mfma_f32_16x16x32_f16 v[206:209], v[78:81], v[34:37], 0
	v_min3_i32 v218, v114, v125, s11
	s_add_i32 s11, s3, 0x500
	s_mov_b32 s12, 0x2aaaaaab
	v_mfma_f32_16x16x32_f16 v[212:215], v[74:77], v[34:37], 0
	s_nop 0
	v_min3_i32 v114, v150, v151, v158
	v_min3_i32 v114, v152, v153, v114
	v_min3_i32 v114, v174, v175, v114
	v_min3_i32 v130, v176, v177, v114
	v_min3_i32 v130, v134, v135, v130
	v_min3_i32 v130, v136, v137, v130
	v_min3_i32 v130, v178, v179, v130
	v_min3_i32 v219, v180, v181, v130
	v_cmp_ge_i32_e32 vcc, v219, v158
	v_mfma_f32_16x16x32_f16 v[224:227], v[94:97], v[30:33], 0
	s_nop 0
	v_cndmask_b32_e32 v221, 1, v159, vcc
	v_mfma_f32_16x16x32_f16 v[228:231], v[78:81], v[30:33], 0
	v_mfma_f32_16x16x32_f16 v[232:235], v[74:77], v[30:33], 0
	s_nop 0
	v_min3_i32 v130, v162, v163, v170
	v_min3_i32 v130, v164, v165, v130
	v_min3_i32 v130, v182, v183, v130
	v_min3_i32 v130, v184, v185, v130
	v_min3_i32 v134, v206, v207, v130
	v_mfma_f32_16x16x32_f16 v[236:239], v[94:97], v[26:29], 0
	v_mfma_f32_16x16x32_f16 v[186:189], v[94:97], v[22:25], 0
	v_mfma_f32_16x16x32_f16 v[146:149], v[94:97], v[18:21], 0
	v_mfma_f32_16x16x32_f16 v[138:141], v[94:97], v[14:17], 0
	v_mfma_f32_16x16x32_f16 v[142:145], v[94:97], v[10:13], 0
	v_mfma_f32_16x16x32_f16 v[126:129], v[94:97], v[6:9], 0
	v_mfma_f32_16x16x32_f16 v[94:97], v[78:81], v[26:29], 0
	v_mfma_f32_16x16x32_f16 v[190:193], v[78:81], v[22:25], 0
	v_mfma_f32_16x16x32_f16 v[174:177], v[78:81], v[18:21], 0
	v_mfma_f32_16x16x32_f16 v[158:161], v[78:81], v[14:17], 0
	v_mfma_f32_16x16x32_f16 v[162:165], v[78:81], v[10:13], 0
	v_mfma_f32_16x16x32_f16 v[130:133], v[78:81], v[6:9], 0
	v_min3_i32 v78, v208, v209, v134
	v_min3_i32 v78, v212, v213, v78
	v_min3_i32 v217, v214, v215, v78
	v_cmp_ge_i32_e32 vcc, v217, v170
	v_mfma_f32_16x16x32_f16 v[122:125], v[74:77], v[26:29], 0
	s_nop 0
	v_cndmask_b32_e32 v222, 1, v171, vcc
	v_mfma_f32_16x16x32_f16 v[114:117], v[74:77], v[22:25], 0
	v_min3_i32 v78, v166, v167, v172
	v_min3_i32 v78, v168, v169, v78
	v_min3_i32 v78, v224, v225, v78
	v_min3_i32 v134, v226, v227, v78
	v_min3_i32 v134, v228, v229, v134
	v_min3_i32 v134, v230, v231, v134
	v_min3_i32 v134, v232, v233, v134
	v_min3_i32 v211, v234, v235, v134
	v_cmp_ge_i32_e32 vcc, v211, v172
	v_mfma_f32_16x16x32_f16 v[182:185], v[74:77], v[18:21], 0
	s_nop 0
	v_cndmask_b32_e32 v213, 1, v173, vcc
	v_mfma_f32_16x16x32_f16 v[178:181], v[74:77], v[14:17], 0
	v_mfma_f32_16x16x32_f16 v[78:81], v[74:77], v[10:13], 0
	v_mfma_f32_16x16x32_f16 v[150:153], v[74:77], v[6:9], 0
	v_min3_i32 v74, v154, v155, v196
	v_min3_i32 v74, v156, v157, v74
	v_min3_i32 v74, v236, v237, v74
	v_min3_i32 v74, v238, v239, v74
	v_min3_i32 v74, v94, v95, v74
	v_min3_i32 v74, v96, v97, v74
	v_min3_i32 v74, v122, v123, v74
	v_min3_i32 v212, v124, v125, v74
	v_cmp_ge_i32_e32 vcc, v212, v196
	s_waitcnt vmcnt(11)
	v_mfma_f32_16x16x32_f16 v[166:169], v[70:73], v[2:5], 0
	v_cndmask_b32_e32 v214, 1, v197, vcc
	v_mfma_f32_16x16x32_f16 v[170:173], v[70:73], v[34:37], 0
	v_min3_i32 v74, v110, v111, v194
	v_min3_i32 v74, v112, v113, v74
	v_min3_i32 v74, v186, v187, v74
	v_min3_i32 v74, v188, v189, v74
	v_min3_i32 v74, v190, v191, v74
	v_min3_i32 v74, v192, v193, v74
	v_min3_i32 v74, v114, v115, v74
	v_min3_i32 v215, v116, v117, v74
	v_cmp_ge_i32_e32 vcc, v215, v194
	v_mfma_f32_16x16x32_f16 v[154:157], v[70:73], v[30:33], 0
	s_nop 0
	v_cndmask_b32_e32 v216, 1, v195, vcc
	v_mfma_f32_16x16x32_f16 v[134:137], v[70:73], v[26:29], 0
	v_min3_i32 v74, v118, v119, v198
	v_min3_i32 v74, v120, v121, v74
	v_mfma_f32_16x16x32_f16 v[122:125], v[70:73], v[22:25], 0
	v_mfma_f32_16x16x32_f16 v[94:97], v[70:73], v[18:21], 0
	v_mfma_f32_16x16x32_f16 v[110:113], v[70:73], v[14:17], 0
	v_mfma_f32_16x16x32_f16 v[114:117], v[70:73], v[10:13], 0
	v_mfma_f32_16x16x32_f16 v[118:121], v[70:73], v[6:9], 0
	v_min3_i32 v70, v146, v147, v74
	v_min3_i32 v70, v148, v149, v70
	v_min3_i32 v70, v174, v175, v70
	v_min3_i32 v70, v176, v177, v70
	v_min3_i32 v70, v182, v183, v70
	v_min3_i32 v223, v184, v185, v70
	v_cmp_ge_i32_e32 vcc, v223, v198
	s_waitcnt vmcnt(10)
	v_mfma_f32_16x16x32_f16 v[186:189], v[66:69], v[2:5], 0
	v_cndmask_b32_e32 v244, 1, v199, vcc
	v_mfma_f32_16x16x32_f16 v[190:193], v[66:69], v[34:37], 0
	v_min3_i32 v70, v102, v103, v203
	v_min3_i32 v70, v104, v105, v70
	v_min3_i32 v70, v138, v139, v70
	v_min3_i32 v70, v140, v141, v70
	v_min3_i32 v70, v158, v159, v70
	v_min3_i32 v70, v160, v161, v70
	v_min3_i32 v70, v178, v179, v70
	v_min3_i32 v245, v180, v181, v70
	v_cmp_ge_i32_e32 vcc, v245, v203
	v_mfma_f32_16x16x32_f16 v[224:227], v[66:69], v[30:33], 0
	s_nop 0
	v_cndmask_b32_e32 v246, 1, v204, vcc
	v_mfma_f32_16x16x32_f16 v[198:201], v[66:69], v[26:29], 0
	v_min3_i32 v70, v106, v107, v202
	v_min3_i32 v70, v108, v109, v70
	v_min3_i32 v70, v142, v143, v70
	v_mfma_f32_16x16x32_f16 v[158:161], v[66:69], v[22:25], 0
	v_min3_i32 v70, v144, v145, v70
	v_min3_i32 v70, v162, v163, v70
	v_min3_i32 v70, v164, v165, v70
	v_mfma_f32_16x16x32_f16 v[146:149], v[66:69], v[18:21], 0
	v_min3_i32 v70, v78, v79, v70
	v_min3_i32 v247, v80, v81, v70
	v_cmp_ge_i32_e32 vcc, v247, v202
	v_mfma_f32_16x16x32_f16 v[138:141], v[66:69], v[14:17], 0
	s_nop 0
	v_cndmask_b32_e32 v248, 1, v205, vcc
	v_mfma_f32_16x16x32_f16 v[106:109], v[66:69], v[10:13], 0
	v_mfma_f32_16x16x32_f16 v[102:105], v[66:69], v[6:9], 0
	v_mov_b32_e32 v66, 0
	s_nop 0
	v_add_u32_e32 v72, v1, v66
	v_add_u32_e32 v66, s11, v72
	s_add_i32 s11, s3, 0x540
	v_add_u32_e32 v68, s11, v72
	s_add_i32 s11, s3, 0x580
	v_add_u32_e32 v70, s11, v72
	s_addk_i32 s3, 0x5c0
	v_ashrrev_i32_e32 v67, 31, v66
	v_ashrrev_i32_e32 v69, 31, v68
	v_ashrrev_i32_e32 v71, 31, v70
	v_add_u32_e32 v72, s3, v72
	s_waitcnt vmcnt(9)
	v_mfma_f32_16x16x32_f16 v[178:181], v[90:93], v[2:5], 0
	v_lshl_add_u64 v[66:67], v[66:67], 4, s[6:7]
	v_lshl_add_u64 v[68:69], v[68:69], 4, s[6:7]
	v_lshl_add_u64 v[70:71], v[70:71], 4, s[6:7]
	s_waitcnt vmcnt(8)
	v_mfma_f32_16x16x32_f16 v[194:197], v[86:89], v[2:5], 0
	v_ashrrev_i32_e32 v73, 31, v72
	v_lshl_add_u64 v[142:143], v[72:73], 4, s[6:7]
	global_load_dwordx4 v[78:81], v[66:67], off nt
	global_load_dwordx4 v[74:77], v[68:69], off nt
	s_nop 0
	global_load_dwordx4 v[70:73], v[70:71], off nt
	s_nop 0
	global_load_dwordx4 v[66:69], v[142:143], off nt
	v_mfma_f32_16x16x32_f16 v[228:231], v[90:93], v[34:37], 0
	v_min3_i32 v98, v98, v99, v218
	v_min3_i32 v98, v100, v101, v98
	v_min3_i32 v98, v126, v127, v98
	v_min3_i32 v98, v128, v129, v98
	v_min3_i32 v98, v130, v131, v98
	v_min3_i32 v98, v132, v133, v98
	v_min3_i32 v98, v150, v151, v98
	v_min3_i32 v249, v152, v153, v98
	v_cmp_ge_i32_e32 vcc, v249, v218
	v_mfma_f32_16x16x32_f16 v[232:235], v[86:89], v[34:37], 0
	s_mul_i32 s3, s15, 6
	v_cndmask_b32_e32 v218, 1, v220, vcc
	v_mfma_f32_16x16x32_f16 v[236:239], v[90:93], v[30:33], 0
	v_min3_i32 v98, v166, v167, v219
	s_mul_i32 s11, s2, 0x90
	v_mfma_f32_16x16x32_f16 v[206:209], v[90:93], v[26:29], 0
	v_mfma_f32_16x16x32_f16 v[182:185], v[90:93], v[22:25], 0
	v_mfma_f32_16x16x32_f16 v[174:177], v[90:93], v[18:21], 0
	v_mfma_f32_16x16x32_f16 v[162:165], v[90:93], v[14:17], 0
	v_mfma_f32_16x16x32_f16 v[142:145], v[90:93], v[10:13], 0
	v_mfma_f32_16x16x32_f16 v[126:129], v[90:93], v[6:9], 0
	v_min3_i32 v90, v168, v169, v98
	v_min3_i32 v90, v186, v187, v90
	v_min3_i32 v98, v188, v189, v90
	v_min3_i32 v98, v178, v179, v98
	v_min3_i32 v98, v180, v181, v98
	v_min3_i32 v98, v194, v195, v98
	v_min3_i32 v220, v196, v197, v98
	v_cmp_ge_i32_e32 vcc, v220, v219
	v_mfma_f32_16x16x32_f16 v[240:243], v[86:89], v[30:33], 0
	s_nop 0
	v_cndmask_b32_e32 v219, 2, v221, vcc
	v_mfma_f32_16x16x32_f16 v[90:93], v[86:89], v[26:29], 0
	v_min3_i32 v98, v170, v171, v217
	v_min3_i32 v98, v172, v173, v98
	v_min3_i32 v98, v190, v191, v98
	v_min3_i32 v98, v192, v193, v98
	v_min3_i32 v98, v228, v229, v98
	v_min3_i32 v98, v230, v231, v98
	v_min3_i32 v98, v232, v233, v98
	v_min3_i32 v221, v234, v235, v98
	v_cmp_ge_i32_e32 vcc, v221, v217
	v_mfma_f32_16x16x32_f16 v[202:205], v[86:89], v[22:25], 0
	s_nop 0
	v_cndmask_b32_e32 v217, 2, v222, vcc
	v_mfma_f32_16x16x32_f16 v[194:197], v[86:89], v[18:21], 0
	v_mfma_f32_16x16x32_f16 v[186:189], v[86:89], v[14:17], 0
	v_mfma_f32_16x16x32_f16 v[166:169], v[86:89], v[10:13], 0
	v_mfma_f32_16x16x32_f16 v[150:153], v[86:89], v[6:9], 0
	v_min3_i32 v86, v154, v155, v211
	v_min3_i32 v86, v156, v157, v86
	v_min3_i32 v86, v224, v225, v86
	v_min3_i32 v86, v226, v227, v86
	v_min3_i32 v86, v236, v237, v86
	v_min3_i32 v86, v238, v239, v86
	v_min3_i32 v86, v240, v241, v86
	v_min3_i32 v222, v242, v243, v86
	v_cmp_ge_i32_e32 vcc, v222, v211
	s_waitcnt vmcnt(11)
	v_mfma_f32_16x16x32_f16 v[170:173], v[50:53], v[2:5], 0
	v_cndmask_b32_e32 v211, 2, v213, vcc
	v_mfma_f32_16x16x32_f16 v[154:157], v[50:53], v[34:37], 0
	v_min3_i32 v86, v134, v135, v212
	v_min3_i32 v86, v136, v137, v86
	v_min3_i32 v86, v198, v199, v86
	v_min3_i32 v86, v200, v201, v86
	v_min3_i32 v86, v206, v207, v86
	v_min3_i32 v86, v208, v209, v86
	v_min3_i32 v86, v90, v91, v86
	v_min3_i32 v198, v92, v93, v86
	v_cmp_ge_i32_e32 vcc, v198, v212
	s_waitcnt vmcnt(10)
	v_mfma_f32_16x16x32_f16 v[134:137], v[46:49], v[2:5], 0
	v_cndmask_b32_e32 v199, 2, v214, vcc
	v_mfma_f32_16x16x32_f16 v[178:181], v[50:53], v[30:33], 0
	v_min3_i32 v122, v122, v123, v215
	v_min3_i32 v122, v124, v125, v122
	v_min3_i32 v122, v158, v159, v122
	v_min3_i32 v122, v160, v161, v122
	v_min3_i32 v122, v182, v183, v122
	v_min3_i32 v122, v184, v185, v122
	v_min3_i32 v122, v202, v203, v122
	v_min3_i32 v200, v204, v205, v122
	v_cmp_ge_i32_e32 vcc, v200, v215
	s_waitcnt vmcnt(9)
	v_mfma_f32_16x16x32_f16 v[158:161], v[42:45], v[2:5], 0
	v_cndmask_b32_e32 v201, 2, v216, vcc
	s_waitcnt vmcnt(8)
	v_mfma_f32_16x16x32_f16 v[182:185], v[38:41], v[2:5], 0
	v_min3_i32 v94, v94, v95, v223
	v_min3_i32 v94, v96, v97, v94
	v_min3_i32 v94, v146, v147, v94
	v_min3_i32 v94, v148, v149, v94
	v_min3_i32 v94, v174, v175, v94
	v_min3_i32 v94, v176, v177, v94
	v_min3_i32 v94, v194, v195, v94
	v_min3_i32 v202, v196, v197, v94
	v_cmp_ge_i32_e32 vcc, v202, v223
	v_mfma_f32_16x16x32_f16 v[146:149], v[46:49], v[34:37], 0
	s_nop 0
	v_cndmask_b32_e32 v203, 2, v244, vcc
	v_mfma_f32_16x16x32_f16 v[174:177], v[42:45], v[34:37], 0
	v_min3_i32 v94, v110, v111, v245
	v_min3_i32 v94, v112, v113, v94
	v_min3_i32 v94, v138, v139, v94
	v_min3_i32 v94, v140, v141, v94
	v_min3_i32 v94, v162, v163, v94
	v_min3_i32 v94, v164, v165, v94
	v_min3_i32 v94, v186, v187, v94
	v_min3_i32 v204, v188, v189, v94
	v_cmp_ge_i32_e32 vcc, v204, v245
	v_mfma_f32_16x16x32_f16 v[194:197], v[38:41], v[34:37], 0
	s_nop 0
	v_cndmask_b32_e32 v205, 2, v246, vcc
	v_mfma_f32_16x16x32_f16 v[110:113], v[46:49], v[30:33], 0
	v_min3_i32 v94, v114, v115, v247
	v_min3_i32 v94, v116, v117, v94
	v_min3_i32 v94, v106, v107, v94
	v_min3_i32 v94, v108, v109, v94
	v_min3_i32 v94, v142, v143, v94
	v_min3_i32 v94, v144, v145, v94
	v_min3_i32 v94, v166, v167, v94
	v_min3_i32 v206, v168, v169, v94
	v_cmp_ge_i32_e32 vcc, v206, v247
	v_mfma_f32_16x16x32_f16 v[190:193], v[50:53], v[26:29], 0
	s_nop 0
	v_cndmask_b32_e32 v207, 2, v248, vcc
	v_mfma_f32_16x16x32_f16 v[138:141], v[46:49], v[26:29], 0
	v_min3_i32 v114, v118, v119, v249
	v_min3_i32 v114, v120, v121, v114
	v_min3_i32 v102, v102, v103, v114
	v_min3_i32 v102, v104, v105, v102
	v_min3_i32 v102, v126, v127, v102
	v_min3_i32 v102, v128, v129, v102
	v_min3_i32 v102, v150, v151, v102
	v_min3_i32 v208, v152, v153, v102
	v_cmp_ge_i32_e32 vcc, v208, v249
	v_mfma_f32_16x16x32_f16 v[118:121], v[42:45], v[30:33], 0
	s_nop 0
	v_cndmask_b32_e32 v209, 2, v218, vcc
	v_mfma_f32_16x16x32_f16 v[126:129], v[38:41], v[30:33], 0
	v_min3_i32 v102, v170, v171, v220
	v_min3_i32 v102, v172, v173, v102
	v_min3_i32 v102, v134, v135, v102
	v_min3_i32 v102, v136, v137, v102
	v_min3_i32 v102, v158, v159, v102
	v_min3_i32 v102, v160, v161, v102
	v_min3_i32 v102, v182, v183, v102
	v_min3_i32 v182, v184, v185, v102
	v_cmp_ge_i32_e32 vcc, v182, v220
	v_mfma_f32_16x16x32_f16 v[142:145], v[42:45], v[26:29], 0
	s_nop 0
	v_cndmask_b32_e32 v183, 3, v219, vcc
	v_mfma_f32_16x16x32_f16 v[150:153], v[38:41], v[26:29], 0
	v_min3_i32 v102, v154, v155, v221
	v_min3_i32 v102, v156, v157, v102
	v_min3_i32 v102, v146, v147, v102
	v_min3_i32 v134, v148, v149, v102
	v_min3_i32 v134, v174, v175, v134
	v_min3_i32 v134, v176, v177, v134
	v_min3_i32 v134, v194, v195, v134
	v_min3_i32 v174, v196, v197, v134
	v_cmp_ge_i32_e32 vcc, v174, v221
	v_mfma_f32_16x16x32_f16 v[130:133], v[50:53], v[22:25], 0
	s_nop 0
	v_cndmask_b32_e32 v175, 3, v217, vcc
	v_mfma_f32_16x16x32_f16 v[186:189], v[46:49], v[22:25], 0
	v_min3_i32 v134, v178, v179, v222
	v_min3_i32 v134, v180, v181, v134
	v_min3_i32 v110, v110, v111, v134
	v_min3_i32 v110, v112, v113, v110
	v_min3_i32 v110, v118, v119, v110
	v_min3_i32 v110, v120, v121, v110
	v_min3_i32 v110, v126, v127, v110
	v_min3_i32 v176, v128, v129, v110
	v_cmp_ge_i32_e32 vcc, v176, v222
	v_mfma_f32_16x16x32_f16 v[166:169], v[42:45], v[22:25], 0
	s_nop 0
	v_cndmask_b32_e32 v177, 3, v211, vcc
	v_mfma_f32_16x16x32_f16 v[170:173], v[38:41], v[22:25], 0
	s_nop 0
	v_min3_i32 v118, v190, v191, v198
	v_mfma_f32_16x16x32_f16 v[162:165], v[38:41], v[18:21], 0
	v_mfma_f32_16x16x32_f16 v[146:149], v[38:41], v[14:17], 0
	v_mfma_f32_16x16x32_f16 v[126:129], v[38:41], v[10:13], 0
	v_mfma_f32_16x16x32_f16 v[110:113], v[38:41], v[6:9], 0
	v_min3_i32 v38, v192, v193, v118
	v_min3_i32 v38, v138, v139, v38
	v_min3_i32 v38, v140, v141, v38
	v_min3_i32 v38, v142, v143, v38
	v_min3_i32 v38, v144, v145, v38
	v_min3_i32 v38, v150, v151, v38
	v_min3_i32 v178, v152, v153, v38
	v_cmp_ge_i32_e32 vcc, v178, v198
	v_mfma_f32_16x16x32_f16 v[98:101], v[50:53], v[18:21], 0
	s_nop 0
	v_cndmask_b32_e32 v179, 3, v199, vcc
	v_mfma_f32_16x16x32_f16 v[122:125], v[46:49], v[18:21], 0
	v_mfma_f32_16x16x32_f16 v[158:161], v[42:45], v[18:21], 0
	s_nop 0
	v_min3_i32 v38, v130, v131, v200
	v_min3_i32 v38, v132, v133, v38
	v_min3_i32 v38, v186, v187, v38
	v_min3_i32 v38, v188, v189, v38
	v_min3_i32 v38, v166, v167, v38
	v_min3_i32 v38, v168, v169, v38
	v_min3_i32 v38, v170, v171, v38
	v_min3_i32 v166, v172, v173, v38
	v_cmp_ge_i32_e32 vcc, v166, v200
	v_mfma_f32_16x16x32_f16 v[86:89], v[50:53], v[14:17], 0
	s_nop 0
	v_cndmask_b32_e32 v167, 3, v201, vcc
	v_mfma_f32_16x16x32_f16 v[106:109], v[46:49], v[14:17], 0
	v_mfma_f32_16x16x32_f16 v[114:117], v[42:45], v[14:17], 0
	s_nop 0
	v_min3_i32 v38, v98, v99, v202
	v_min3_i32 v38, v100, v101, v38
	v_min3_i32 v38, v122, v123, v38
	v_min3_i32 v38, v124, v125, v38
	v_min3_i32 v38, v158, v159, v38
	v_min3_i32 v38, v160, v161, v38
	v_min3_i32 v122, v162, v163, v38
	v_min3_i32 v158, v164, v165, v122
	v_cmp_ge_i32_e32 vcc, v158, v202
	v_mfma_f32_16x16x32_f16 v[90:93], v[50:53], v[10:13], 0
	s_nop 0
	v_cndmask_b32_e32 v159, 3, v203, vcc
	v_mfma_f32_16x16x32_f16 v[94:97], v[46:49], v[10:13], 0
	v_mfma_f32_16x16x32_f16 v[102:105], v[42:45], v[10:13], 0
	s_nop 0
	v_min3_i32 v86, v86, v87, v204
	v_min3_i32 v122, v88, v89, v86
	v_min3_i32 v106, v106, v107, v122
	v_min3_i32 v106, v108, v109, v106
	v_min3_i32 v114, v114, v115, v106
	v_min3_i32 v114, v116, v117, v114
	v_min3_i32 v114, v146, v147, v114
	v_min3_i32 v146, v148, v149, v114
	v_cmp_ge_i32_e32 vcc, v146, v204
	v_mfma_f32_16x16x32_f16 v[50:53], v[50:53], v[6:9], 0
	s_nop 0
	v_cndmask_b32_e32 v147, 3, v205, vcc
	v_mfma_f32_16x16x32_f16 v[46:49], v[46:49], v[6:9], 0
	v_mfma_f32_16x16x32_f16 v[42:45], v[42:45], v[6:9], 0
	s_nop 0
	v_min3_i32 v90, v90, v91, v206
	v_min3_i32 v90, v92, v93, v90
	v_min3_i32 v90, v94, v95, v90
	v_min3_i32 v94, v96, v97, v90
	v_min3_i32 v94, v102, v103, v94
	v_min3_i32 v94, v104, v105, v94
	v_min3_i32 v102, v126, v127, v94
	v_min3_i32 v148, v128, v129, v102
	v_cmp_ge_i32_e32 vcc, v148, v206
	s_waitcnt vmcnt(7)
	v_mfma_f32_16x16x32_f16 v[134:137], v[82:85], v[2:5], 0
	v_cndmask_b32_e32 v149, 3, v207, vcc
	v_mfma_f32_16x16x32_f16 v[138:141], v[82:85], v[34:37], 0
	v_mfma_f32_16x16x32_f16 v[142:145], v[82:85], v[30:33], 0
	v_mfma_f32_16x16x32_f16 v[150:153], v[82:85], v[26:29], 0
	v_mfma_f32_16x16x32_f16 v[154:157], v[82:85], v[22:25], 0
	v_mfma_f32_16x16x32_f16 v[130:133], v[82:85], v[18:21], 0
	v_mfma_f32_16x16x32_f16 v[118:121], v[82:85], v[14:17], 0
	v_mfma_f32_16x16x32_f16 v[98:101], v[82:85], v[10:13], 0
	v_mfma_f32_16x16x32_f16 v[38:41], v[82:85], v[6:9], 0
	s_waitcnt vmcnt(6)
	v_mfma_f32_16x16x32_f16 v[82:85], v[62:65], v[2:5], 0
	s_waitcnt vmcnt(5)
	v_mfma_f32_16x16x32_f16 v[86:89], v[58:61], v[2:5], 0
	s_waitcnt vmcnt(4)
	v_mfma_f32_16x16x32_f16 v[106:109], v[54:57], v[2:5], 0
	s_nop 0
	v_min3_i32 v50, v50, v51, v208
	v_min3_i32 v126, v52, v53, v50
	v_min3_i32 v46, v46, v47, v126
	v_min3_i32 v46, v48, v49, v46
	v_min3_i32 v42, v42, v43, v46
	v_min3_i32 v42, v44, v45, v42
	v_min3_i32 v42, v110, v111, v42
	v_min3_i32 v160, v112, v113, v42
	v_cmp_ge_i32_e32 vcc, v160, v208
	v_mfma_f32_16x16x32_f16 v[114:117], v[62:65], v[34:37], 0
	s_nop 0
	v_cndmask_b32_e32 v161, 3, v209, vcc
	v_mfma_f32_16x16x32_f16 v[122:125], v[58:61], v[34:37], 0
	v_mfma_f32_16x16x32_f16 v[90:93], v[54:57], v[34:37], 0
	s_nop 0
	v_min3_i32 v42, v134, v135, v182
	v_min3_i32 v42, v136, v137, v42
	v_min3_i32 v42, v82, v83, v42
	v_min3_i32 v42, v84, v85, v42
	v_min3_i32 v42, v86, v87, v42
	v_min3_i32 v42, v88, v89, v42
	v_min3_i32 v42, v106, v107, v42
	v_min3_i32 v134, v108, v109, v42
	v_cmp_ge_i32_e32 vcc, v134, v182
	v_mfma_f32_16x16x32_f16 v[94:97], v[62:65], v[30:33], 0
	s_nop 0
	v_cndmask_b32_e32 v135, 4, v183, vcc
	v_mfma_f32_16x16x32_f16 v[102:105], v[58:61], v[30:33], 0
	v_mfma_f32_16x16x32_f16 v[50:53], v[54:57], v[30:33], 0
	v_mfma_f32_16x16x32_f16 v[46:49], v[62:65], v[26:29], 0
	v_mfma_f32_16x16x32_f16 v[110:113], v[62:65], v[22:25], 0
	v_mfma_f32_16x16x32_f16 v[126:129], v[62:65], v[18:21], 0
	v_mfma_f32_16x16x32_f16 v[82:85], v[62:65], v[14:17], 0
	v_mfma_f32_16x16x32_f16 v[86:89], v[62:65], v[10:13], 0
	v_mfma_f32_16x16x32_f16 v[42:45], v[62:65], v[6:9], 0
	v_min3_i32 v62, v138, v139, v174
	v_min3_i32 v106, v140, v141, v62
	v_min3_i32 v106, v114, v115, v106
	v_min3_i32 v106, v116, v117, v106
	v_min3_i32 v114, v122, v123, v106
	v_min3_i32 v114, v124, v125, v114
	v_min3_i32 v90, v90, v91, v114
	v_min3_i32 v122, v92, v93, v90
	v_cmp_ge_i32_e32 vcc, v122, v174
	v_mfma_f32_16x16x32_f16 v[62:65], v[58:61], v[26:29], 0
	s_nop 0
	v_cndmask_b32_e32 v123, 4, v175, vcc
	v_mfma_f32_16x16x32_f16 v[106:109], v[54:57], v[26:29], 0
	s_nop 0
	v_min3_i32 v124, v142, v143, v176
	v_min3_i32 v124, v144, v145, v124
	v_min3_i32 v94, v94, v95, v124
	v_min3_i32 v124, v96, v97, v94
	v_min3_i32 v102, v102, v103, v124
	v_min3_i32 v102, v104, v105, v102
	v_min3_i32 v50, v50, v51, v102
	v_min3_i32 v124, v52, v53, v50
	v_cmp_ge_i32_e32 vcc, v124, v176
	v_mfma_f32_16x16x32_f16 v[90:93], v[58:61], v[22:25], 0
	s_nop 0
	v_cndmask_b32_e32 v125, 4, v177, vcc
	v_mfma_f32_16x16x32_f16 v[114:117], v[54:57], v[22:25], 0
	s_nop 0
	v_min3_i32 v136, v150, v151, v178
	v_min3_i32 v136, v152, v153, v136
	v_min3_i32 v46, v46, v47, v136
	v_min3_i32 v46, v48, v49, v46
	v_min3_i32 v62, v62, v63, v46
	v_min3_i32 v62, v64, v65, v62
	v_min3_i32 v62, v106, v107, v62
	v_min3_i32 v136, v108, v109, v62
	v_cmp_ge_i32_e32 vcc, v136, v178
	v_mfma_f32_16x16x32_f16 v[94:97], v[58:61], v[18:21], 0
	s_nop 0
	v_cndmask_b32_e32 v137, 4, v179, vcc
	v_mfma_f32_16x16x32_f16 v[46:49], v[54:57], v[18:21], 0
	s_nop 0
	v_min3_i32 v138, v154, v155, v166
	v_min3_i32 v138, v156, v157, v138
	v_min3_i32 v110, v110, v111, v138
	v_min3_i32 v110, v112, v113, v110
	v_min3_i32 v90, v90, v91, v110
	v_min3_i32 v90, v92, v93, v90
	v_min3_i32 v110, v114, v115, v90
	v_min3_i32 v138, v116, v117, v110
	v_cmp_ge_i32_e32 vcc, v138, v166
	v_mfma_f32_16x16x32_f16 v[102:105], v[58:61], v[14:17], 0
	v_mov_b32_e32 v154, 0
	v_cndmask_b32_e32 v139, 4, v167, vcc
	v_mfma_f32_16x16x32_f16 v[62:65], v[54:57], v[14:17], 0
	s_nop 0
	v_min3_i32 v114, v130, v131, v158
	v_min3_i32 v130, v132, v133, v114
	v_min3_i32 v126, v126, v127, v130
	v_min3_i32 v126, v128, v129, v126
	v_min3_i32 v94, v94, v95, v126
	v_min3_i32 v94, v96, v97, v94
	v_min3_i32 v46, v46, v47, v94
	v_min3_i32 v126, v48, v49, v46
	v_cmp_ge_i32_e32 vcc, v126, v158
	v_mfma_f32_16x16x32_f16 v[50:53], v[58:61], v[10:13], 0
	s_nop 0
	v_cndmask_b32_e32 v127, 4, v159, vcc
	v_mfma_f32_16x16x32_f16 v[106:109], v[54:57], v[10:13], 0
	s_nop 0
	v_min3_i32 v118, v118, v119, v146
	v_min3_i32 v118, v120, v121, v118
	v_min3_i32 v82, v82, v83, v118
	v_min3_i32 v118, v84, v85, v82
	v_min3_i32 v102, v102, v103, v118
	v_min3_i32 v102, v104, v105, v102
	v_min3_i32 v62, v62, v63, v102
	v_min3_i32 v102, v64, v65, v62
	v_cmp_ge_i32_e32 vcc, v102, v146
	v_mfma_f32_16x16x32_f16 v[58:61], v[58:61], v[6:9], 0
	v_and_b32_e32 v146, 7, v0
	v_cndmask_b32_e32 v103, 4, v147, vcc
	v_mfma_f32_16x16x32_f16 v[54:57], v[54:57], v[6:9], 0
	s_nop 0
	v_min3_i32 v98, v98, v99, v148
	v_min3_i32 v104, v100, v101, v98
	v_min3_i32 v86, v86, v87, v104
	v_min3_i32 v86, v88, v89, v86
	v_min3_i32 v50, v50, v51, v86
	v_min3_i32 v50, v52, v53, v50
	v_min3_i32 v50, v106, v107, v50
	v_min3_i32 v104, v108, v109, v50
	v_cmp_ge_i32_e32 vcc, v104, v148
	s_waitcnt vmcnt(3)
	v_mfma_f32_16x16x32_f16 v[90:93], v[78:81], v[2:5], 0
	v_cndmask_b32_e32 v105, 4, v149, vcc
	s_waitcnt vmcnt(2)
	v_mfma_f32_16x16x32_f16 v[110:113], v[74:77], v[2:5], 0
	s_waitcnt vmcnt(1)
	v_mfma_f32_16x16x32_f16 v[114:117], v[70:73], v[2:5], 0
	s_waitcnt vmcnt(0)
	v_mfma_f32_16x16x32_f16 v[2:5], v[66:69], v[2:5], 0
	s_nop 0
	v_min3_i32 v38, v38, v39, v160
	v_min3_i32 v38, v40, v41, v38
	v_min3_i32 v38, v42, v43, v38
	v_min3_i32 v42, v44, v45, v38
	v_min3_i32 v42, v58, v59, v42
	v_min3_i32 v42, v60, v61, v42
	v_min3_i32 v54, v54, v55, v42
	v_min3_i32 v106, v56, v57, v54
	v_cmp_ge_i32_e32 vcc, v106, v160
	v_mfma_f32_16x16x32_f16 v[46:49], v[78:81], v[34:37], 0
	s_nop 0
	v_cndmask_b32_e32 v107, 4, v161, vcc
	v_mfma_f32_16x16x32_f16 v[94:97], v[74:77], v[34:37], 0
	v_mfma_f32_16x16x32_f16 v[82:85], v[70:73], v[34:37], 0
	v_mfma_f32_16x16x32_f16 v[34:37], v[66:69], v[34:37], 0
	s_nop 0
	v_min3_i32 v54, v90, v91, v134
	v_min3_i32 v58, v92, v93, v54
	v_min3_i32 v58, v110, v111, v58
	v_min3_i32 v58, v112, v113, v58
	v_min3_i32 v90, v114, v115, v58
	v_min3_i32 v90, v116, v117, v90
	v_min3_i32 v2, v2, v3, v90
	v_min3_i32 v91, v4, v5, v2
	v_cmp_ge_i32_e32 vcc, v91, v134
	v_mfma_f32_16x16x32_f16 v[62:65], v[78:81], v[30:33], 0
	s_nop 0
	v_cndmask_b32_e32 v90, 5, v135, vcc
	v_add_u32_e32 v251, s3, v90
	v_lshl_or_b32 v90, v251, 2, v253
	ds_min_u64 v252, v[90:91] offset:16384
	v_mfma_f32_16x16x32_f16 v[98:101], v[74:77], v[30:33], 0
	v_mfma_f32_16x16x32_f16 v[86:89], v[70:73], v[30:33], 0
	v_mfma_f32_16x16x32_f16 v[30:33], v[66:69], v[30:33], 0
	s_nop 0
	v_min3_i32 v46, v46, v47, v122
	v_min3_i32 v46, v48, v49, v46
	v_min3_i32 v46, v94, v95, v46
	v_min3_i32 v92, v96, v97, v46
	v_min3_i32 v82, v82, v83, v92
	v_min3_i32 v82, v84, v85, v82
	v_min3_i32 v34, v34, v35, v82
	v_min3_i32 v93, v36, v37, v34
	v_cmp_ge_i32_e32 vcc, v93, v122
	v_mfma_f32_16x16x32_f16 v[50:53], v[78:81], v[26:29], 0
	s_nop 0
	v_cndmask_b32_e32 v92, 5, v123, vcc
	v_add_u32_e32 v251, s3, v92
	v_lshl_or_b32 v92, v251, 2, v253
	ds_min_u64 v252, v[92:93] offset:16512
	v_mfma_f32_16x16x32_f16 v[38:41], v[74:77], v[26:29], 0
	v_mfma_f32_16x16x32_f16 v[42:45], v[70:73], v[26:29], 0
	v_mfma_f32_16x16x32_f16 v[26:29], v[66:69], v[26:29], 0
	s_nop 0
	v_min3_i32 v62, v62, v63, v124
	v_min3_i32 v62, v64, v65, v62
	v_min3_i32 v62, v98, v99, v62
	v_min3_i32 v62, v100, v101, v62
	v_min3_i32 v86, v86, v87, v62
	v_min3_i32 v86, v88, v89, v86
	v_min3_i32 v30, v30, v31, v86
	v_min3_i32 v95, v32, v33, v30
	v_cmp_ge_i32_e32 vcc, v95, v124
	v_mfma_f32_16x16x32_f16 v[54:57], v[78:81], v[22:25], 0
	s_nop 0
	v_cndmask_b32_e32 v94, 5, v125, vcc
	v_add_u32_e32 v251, s3, v94
	v_lshl_or_b32 v94, v251, 2, v253
	ds_min_u64 v252, v[94:95] offset:16640
	v_mfma_f32_16x16x32_f16 v[58:61], v[74:77], v[22:25], 0
	v_mfma_f32_16x16x32_f16 v[2:5], v[70:73], v[22:25], 0
	v_mfma_f32_16x16x32_f16 v[22:25], v[66:69], v[22:25], 0
	s_nop 0
	v_min3_i32 v50, v50, v51, v136
	v_min3_i32 v50, v52, v53, v50
	v_min3_i32 v38, v38, v39, v50
	v_min3_i32 v38, v40, v41, v38
	v_min3_i32 v38, v42, v43, v38
	v_min3_i32 v38, v44, v45, v38
	v_min3_i32 v26, v26, v27, v38
	v_min3_i32 v51, v28, v29, v26
	v_cmp_ge_i32_e32 vcc, v51, v136
	v_mfma_f32_16x16x32_f16 v[46:49], v[78:81], v[18:21], 0
	s_nop 0
	v_cndmask_b32_e32 v50, 5, v137, vcc
	v_add_u32_e32 v251, s3, v50
	v_lshl_or_b32 v50, v251, 2, v253
	ds_min_u64 v252, v[50:51] offset:16768
	v_mfma_f32_16x16x32_f16 v[82:85], v[74:77], v[18:21], 0
	v_mfma_f32_16x16x32_f16 v[34:37], v[70:73], v[18:21], 0
	v_mfma_f32_16x16x32_f16 v[18:21], v[66:69], v[18:21], 0
	s_nop 0
	v_min3_i32 v42, v54, v55, v138
	v_min3_i32 v52, v56, v57, v42
	v_min3_i32 v52, v58, v59, v52
	v_min3_i32 v52, v60, v61, v52
	v_min3_i32 v2, v2, v3, v52
	v_min3_i32 v2, v4, v5, v2
	v_min3_i32 v2, v22, v23, v2
	v_min3_i32 v53, v24, v25, v2
	v_cmp_ge_i32_e32 vcc, v53, v138
	v_mfma_f32_16x16x32_f16 v[62:65], v[78:81], v[14:17], 0
	s_nop 0
	v_cndmask_b32_e32 v52, 5, v139, vcc
	v_add_u32_e32 v251, s3, v52
	v_lshl_or_b32 v52, v251, 2, v253
	ds_min_u64 v252, v[52:53] offset:16896
	v_mfma_f32_16x16x32_f16 v[30:33], v[74:77], v[14:17], 0
	v_mfma_f32_16x16x32_f16 v[86:89], v[70:73], v[14:17], 0
	v_mfma_f32_16x16x32_f16 v[14:17], v[66:69], v[14:17], 0
	s_nop 0
	v_min3_i32 v46, v46, v47, v126
	v_min3_i32 v46, v48, v49, v46
	v_min3_i32 v54, v82, v83, v46
	v_min3_i32 v54, v84, v85, v54
	v_min3_i32 v34, v34, v35, v54
	v_min3_i32 v34, v36, v37, v34
	v_min3_i32 v18, v18, v19, v34
	v_min3_i32 v19, v20, v21, v18
	v_cmp_ge_i32_e32 vcc, v19, v126
	v_mfma_f32_16x16x32_f16 v[38:41], v[78:81], v[10:13], 0
	s_nop 0
	v_cndmask_b32_e32 v18, 5, v127, vcc
	v_add_u32_e32 v251, s3, v18
	v_lshl_or_b32 v18, v251, 2, v253
	ds_min_u64 v252, v[18:19] offset:17024
	v_mfma_f32_16x16x32_f16 v[26:29], v[74:77], v[10:13], 0
	v_mfma_f32_16x16x32_f16 v[42:45], v[70:73], v[10:13], 0
	v_mfma_f32_16x16x32_f16 v[10:13], v[66:69], v[10:13], 0
	s_nop 0
	v_min3_i32 v20, v62, v63, v102
	v_min3_i32 v20, v64, v65, v20
	v_min3_i32 v20, v30, v31, v20
	v_min3_i32 v20, v32, v33, v20
	v_min3_i32 v20, v86, v87, v20
	v_min3_i32 v20, v88, v89, v20
	v_min3_i32 v14, v14, v15, v20
	v_min3_i32 v15, v16, v17, v14
	v_cmp_ge_i32_e32 vcc, v15, v102
	v_mfma_f32_16x16x32_f16 v[2:5], v[78:81], v[6:9], 0
	v_bfe_u32 v17, v0, 4, 2
	v_cndmask_b32_e32 v14, 5, v103, vcc
	v_add_u32_e32 v251, s3, v14
	v_lshl_or_b32 v14, v251, 2, v253
	ds_min_u64 v252, v[14:15] offset:17152
	v_mfma_f32_16x16x32_f16 v[22:25], v[74:77], v[6:9], 0
	v_mfma_f32_16x16x32_f16 v[46:49], v[70:73], v[6:9], 0
	v_mfma_f32_16x16x32_f16 v[6:9], v[66:69], v[6:9], 0
	s_nop 0
	v_min3_i32 v16, v38, v39, v104
	v_min3_i32 v16, v40, v41, v16
	v_min3_i32 v16, v26, v27, v16
	v_min3_i32 v2, v2, v3, v106
	v_min3_i32 v16, v28, v29, v16
	v_min3_i32 v2, v4, v5, v2
	v_min3_i32 v16, v42, v43, v16
	v_min3_i32 v2, v22, v23, v2
	v_lshlrev_b32_e32 v4, 3, v210
	v_min3_i32 v16, v44, v45, v16
	v_min3_i32 v2, v24, v25, v2
	v_min3_i32 v10, v10, v11, v16
	v_min3_i32 v2, v46, v47, v2
	v_min3_i32 v11, v12, v13, v10
	v_min3_i32 v2, v48, v49, v2
	v_cmp_ge_i32_e32 vcc, v11, v104
	v_min3_i32 v2, v6, v7, v2
	v_cndmask_b32_e32 v10, 5, v105, vcc
	v_add_u32_e32 v251, s3, v10
	v_lshl_or_b32 v10, v251, 2, v253
	ds_min_u64 v252, v[10:11] offset:17280
	v_min3_i32 v3, v8, v9, v2
	v_cmp_ge_i32_e32 vcc, v3, v106
	v_cndmask_b32_e32 v2, 5, v107, vcc
	v_add_u32_e32 v2, s3, v2
	v_bfe_u32 v10, v0, 3, 3
	s_lshl_b32 s3, s15, 3
	v_lshl_or_b32 v2, v2, 2, v17
	v_or_b32_e32 v151, s3, v10
	ds_min_u64 v4, v[2:3] offset:17408
	v_lshlrev_b32_e32 v2, 3, v151
	s_waitcnt lgkmcnt(0)
	s_barrier
	ds_read2st64_b32 v[4:5], v2 offset0:64 offset1:66
	s_add_i32 s2, s3, s11
	s_lshr_b32 s2, s2, 4
	s_add_i32 s2, s2, s8
	s_waitcnt lgkmcnt(0)
	v_ashrrev_i32_e32 v3, 2, v4
	v_mul_hi_i32 v6, v3, s12
	v_lshrrev_b32_e32 v7, 31, v6
	v_add_u32_e32 v6, v6, v7
	v_mul_lo_u32 v7, v6, -6
	v_mul_lo_u32 v6, v6, 24
	v_min_i32_e32 v6, 0xa5, v6
	v_add_lshl_u32 v7, v7, v3, 2
	v_bfe_u32 v3, v0, 2, 1
	v_add3_u32 v152, v6, v3, v7
	v_lshlrev_b32_e32 v6, 2, v4
	v_and_b32_e32 v4, 3, v0
	v_and_or_b32 v153, v6, 12, v4
	v_add_u32_e32 v6, s9, v152
	v_lshl_or_b32 v6, v6, 6, v153
	v_bitop3_b32 v7, s3, 15, v10 bitop3:0xc8
	v_lshl_or_b32 v7, v4, 4, v7
	v_lshl_or_b32 v8, s2, 6, v7
	v_ashrrev_i32_e32 v7, 31, v6
	v_lshl_add_u64 v[6:7], v[6:7], 4, s[6:7]
	v_ashrrev_i32_e32 v9, 31, v8
	v_lshl_add_u64 v[8:9], v[8:9], 4, s[4:5]
	global_load_dwordx4 v[126:129], v[6:7], off
	global_load_dwordx4 v[114:117], v[6:7], off offset:256
	global_load_dwordx4 v[130:133], v[6:7], off offset:2048
	global_load_dwordx4 v[118:121], v[6:7], off offset:2304
	global_load_dwordx4 v[134:137], v[8:9], off
	global_load_dwordx4 v[102:105], v[6:7], off offset:512
	global_load_dwordx4 v[78:81], v[6:7], off offset:768
	global_load_dwordx4 v[106:109], v[6:7], off offset:2560
	global_load_dwordx4 v[82:85], v[6:7], off offset:2816
	v_ashrrev_i32_e32 v6, 2, v5
	v_mul_hi_i32 v7, v6, s12
	v_lshrrev_b32_e32 v11, 31, v7
	v_add_u32_e32 v7, v7, v11
	v_mul_lo_u32 v11, v7, -6
	v_mul_lo_u32 v7, v7, 24
	s_add_i32 s2, s3, 64
	v_min_i32_e32 v7, 0xa5, v7
	v_add_lshl_u32 v6, v11, v6, 2
	s_add_i32 s3, s2, s11
	v_add3_u32 v148, v7, v3, v6
	v_lshlrev_b32_e32 v5, 2, v5
	v_and_or_b32 v149, v5, 12, v4
	v_add_u32_e32 v5, s9, v148
	s_lshr_b32 s3, s3, 4
	v_lshl_or_b32 v6, v5, 6, v149
	s_add_i32 s3, s3, s8
	v_bitop3_b32 v5, s2, 15, v10 bitop3:0xc8
	v_lshl_or_b32 v5, v4, 4, v5
	v_lshl_or_b32 v10, s3, 6, v5
	v_ashrrev_i32_e32 v7, 31, v6
	v_ashrrev_i32_e32 v11, 31, v10
	v_lshl_add_u64 v[6:7], v[6:7], 4, s[6:7]
	v_lshl_add_u64 v[10:11], v[10:11], 4, s[4:5]
	global_load_dwordx4 v[110:113], v[10:11], off
	global_load_dwordx4 v[90:93], v[6:7], off
	global_load_dwordx4 v[62:65], v[6:7], off offset:256
	global_load_dwordx4 v[94:97], v[6:7], off offset:2048
	global_load_dwordx4 v[66:69], v[6:7], off offset:2304
	global_load_dwordx4 v[38:41], v[6:7], off offset:512
	global_load_dwordx4 v[18:21], v[6:7], off offset:768
	global_load_dwordx4 v[42:45], v[6:7], off offset:2560
	global_load_dwordx4 v[22:25], v[6:7], off offset:2816
	s_cmpk_lt_u32 s10, 0x80
	s_cselect_b64 s[2:3], -1, 0
	s_cmpk_gt_u32 s10, 0x7f
	s_cbranch_scc1 .LBB1_4
	v_add_u32_e32 v2, 0x4000, v2
	ds_read_b32 v2, v2 offset:1024
	v_or_b32_e32 v147, 0x80, v151
	v_add_u32_e32 v5, s11, v147
	s_waitcnt lgkmcnt(0)
	v_ashrrev_i32_e32 v6, 2, v2
	v_mul_hi_i32 v7, v6, s12
	v_lshrrev_b32_e32 v8, 31, v7
	v_add_u32_e32 v7, v7, v8
	v_mul_lo_u32 v8, v7, -6
	v_mul_lo_u32 v7, v7, 24
	v_min_i32_e32 v7, 0xa5, v7
	v_add_lshl_u32 v6, v8, v6, 2
	v_add3_u32 v150, v7, v3, v6
	v_lshlrev_b32_e32 v2, 2, v2
	v_lshrrev_b32_e32 v3, 4, v5
	v_and_or_b32 v155, v2, 12, v4
	v_add_u32_e32 v2, s9, v150
	v_add_u32_e32 v3, s8, v3
	v_lshl_or_b32 v2, v2, 6, v155
	v_lshl_or_b32 v4, v4, 4, v151
	v_lshl_or_b32 v4, v3, 6, v4
	v_ashrrev_i32_e32 v3, 31, v2
	v_ashrrev_i32_e32 v5, 31, v4
	v_lshl_add_u64 v[2:3], v[2:3], 4, s[6:7]
	v_lshl_add_u64 v[50:51], v[4:5], 4, s[4:5]
	global_load_dwordx4 v[58:61], v[2:3], off
	global_load_dwordx4 v[46:49], v[2:3], off offset:256
	global_load_dwordx4 v[34:37], v[2:3], off offset:2048
	global_load_dwordx4 v[10:13], v[2:3], off offset:2304
	global_load_dwordx4 v[98:101], v[50:51], off
	global_load_dwordx4 v[30:33], v[2:3], off offset:512
	global_load_dwordx4 v[14:17], v[2:3], off offset:768
	global_load_dwordx4 v[6:9], v[2:3], off offset:2560
	s_nop 0
	global_load_dwordx4 v[2:5], v[2:3], off offset:2816
	s_nop 0
	s_nop 0
	v_lshl_or_b32 v150, v150, 4, v155
	s_branch .LBB1_5

	.amdhsa_kernel _ZN12_GLOBAL__N_113search_kernelEPKfS1_PhPf
		.amdhsa_group_segment_fixed_size 26336
		.amdhsa_private_segment_fixed_size 0
		.amdhsa_kernarg_size 32
		.amdhsa_user_sgpr_count 2
		.amdhsa_user_sgpr_dispatch_ptr 0
		.amdhsa_user_sgpr_queue_ptr 0
		.amdhsa_user_sgpr_kernarg_segment_ptr 1
		.amdhsa_user_sgpr_dispatch_id 0
		.amdhsa_user_sgpr_kernarg_preload_length 0
		.amdhsa_user_sgpr_kernarg_preload_offset 0
		.amdhsa_user_sgpr_private_segment_size 0
		.amdhsa_uses_dynamic_stack 0
		.amdhsa_enable_private_segment 0
		.amdhsa_system_sgpr_workgroup_id_x 1
		.amdhsa_system_sgpr_workgroup_id_y 0
		.amdhsa_system_sgpr_workgroup_id_z 0
		.amdhsa_system_sgpr_workgroup_info 0
		.amdhsa_system_vgpr_workitem_id 0
		.amdhsa_next_free_vgpr 256
		.amdhsa_next_free_sgpr 30
		.amdhsa_accum_offset 256
		.amdhsa_reserve_vcc 1
		.amdhsa_float_round_mode_32 0
		.amdhsa_float_round_mode_16_64 0
		.amdhsa_float_denorm_mode_32 3
		.amdhsa_float_denorm_mode_16_64 3
		.amdhsa_dx10_clamp 1
		.amdhsa_ieee_mode 1
		.amdhsa_fp16_overflow 0
		.amdhsa_tg_split 0
		.amdhsa_exception_fp_ieee_invalid_op 0
		.amdhsa_exception_fp_denorm_src 0
		.amdhsa_exception_fp_ieee_div_zero 0
		.amdhsa_exception_fp_ieee_overflow 0
		.amdhsa_exception_fp_ieee_underflow 0
		.amdhsa_exception_fp_ieee_inexact 0
		.amdhsa_exception_int_div_zero 0
	.end_amdhsa_kernel

amdhsa.kernels:
  - .agpr_count:     0
    .args:
      - .actual_access:  read_only
        .address_space:  global
        .offset:         0
        .size:           8
        .value_kind:     global_buffer
      - .actual_access:  read_only
        .address_space:  global
        .offset:         8
        .size:           8
        .value_kind:     global_buffer
      - .actual_access:  write_only
        .address_space:  global
        .offset:         16
        .size:           8
        .value_kind:     global_buffer
    .group_segment_fixed_size: 26112
    .kernarg_segment_align: 8
    .kernarg_segment_size: 24
    .language:       OpenCL C
    .language_version:
      - 2
      - 0
    .max_flat_workgroup_size: 256
    .name:           _ZN12_GLOBAL__N_111prep_kernelEPKfS1_Ph
    .private_segment_fixed_size: 0
    .sgpr_count:     25
    .sgpr_spill_count: 0
    .symbol:         _ZN12_GLOBAL__N_111prep_kernelEPKfS1_Ph.kd
    .uniform_work_group_size: 1
    .uses_dynamic_stack: false
    .vgpr_count:     34
    .vgpr_spill_count: 0
    .wavefront_size: 64
  - .agpr_count:     0
    .args:
      - .actual_access:  read_only
        .address_space:  global
        .offset:         0
        .size:           8
        .value_kind:     global_buffer
      - .actual_access:  read_only
        .address_space:  global
        .offset:         8
        .size:           8
        .value_kind:     global_buffer
      - .address_space:  global
        .offset:         16
        .size:           8
        .value_kind:     global_buffer
      - .actual_access:  write_only
        .address_space:  global
        .offset:         24
        .size:           8
        .value_kind:     global_buffer
    .group_segment_fixed_size: 26336
    .kernarg_segment_align: 8
    .kernarg_segment_size: 32
    .language:       OpenCL C
    .language_version:
      - 2
      - 0
    .max_flat_workgroup_size: 512
    .name:           _ZN12_GLOBAL__N_113search_kernelEPKfS1_PhPf
    .private_segment_fixed_size: 0
    .sgpr_count:     36
    .sgpr_spill_count: 0
    .symbol:         _ZN12_GLOBAL__N_113search_kernelEPKfS1_PhPf.kd
    .uniform_work_group_size: 1
    .uses_dynamic_stack: false
    .vgpr_count:     256
    .vgpr_spill_count: 0
    .wavefront_size: 64
